# baseline (speedup 1.0000x reference)
_Z16sum_layer_kernelPKfS0_Pf:
	s_load_dwordx4 s[4:7], s[0:1], 0x0
	s_load_dwordx2 s[8:9], s[0:1], 0x10
	s_and_b32 s40, s2, 7
	s_lshr_b32 s41, s2, 3
	s_and_b32 s42, s41, 15
	s_and_b32 s43, s40, 1
	s_lshl_b32 s43, s43, 4
	s_or_b32 s42, s42, s43
	s_lshr_b32 s43, s40, 1
	s_xor_b32 s43, s43, s41
	s_and_b32 s43, s43, 3
	s_lshl_b32 s43, s43, 5
	s_or_b32 s42, s42, s43
	s_lshr_b32 s43, s41, 4
	s_lshl_b32 s43, s43, 7
	s_or_b32 s2, s42, s43
	v_and_b32_e32 v40, 31, v0
	v_bfe_u32 v41, v0, 5, 1
	v_lshrrev_b32_e32 v42, 6, v0
	v_and_b32_e32 v43, 7, v0
	v_bfe_u32 v44, v0, 3, 3
	v_and_b32_e32 v45, 63, v0
	s_lshl_b32 s3, s2, 12
	s_lshl_b32 s19, s2, 7
	v_lshlrev_b32_e32 v1, 11, v41
	v_lshl_or_b32 v1, v40, 2, v1
	v_lshlrev_b32_e32 v46, 4, v43
	v_lshl_add_u32 v35, v44, 16, v46
	v_lshl_add_u32 v35, v42, 21, v35
	v_add_u32_e32 v35, s19, v35
	v_lshlrev_b32_e32 v36, 2, v40
	v_lshl_add_u32 v36, v41, 18, v36
	v_lshl_add_u32 v36, v42, 21, v36
	v_add_u32_e32 v36, s19, v36
	v_mul_u32_u24_e32 v37, 0x1200, v42
	v_mul_u32_u24_e32 v38, 0x90, v44
	v_add3_u32 v38, v37, v38, v46
	v_mul_u32_u24_e32 v39, 0x90, v40
	v_lshlrev_b32_e32 v47, 6, v41
	v_add3_u32 v39, v37, v39, v47
	v_lshrrev_b32_e32 v46, 1, v44
	v_xor_b32_e32 v46, v43, v46
	v_lshlrev_b32_e32 v46, 4, v46
	v_lshl_add_u32 v35, v44, 16, v46
	v_lshl_add_u32 v35, v42, 21, v35
	v_add_u32_e32 v35, s19, v35
	v_xor_b32_e32 v86, 64, v35
	v_readfirstlane_b32 s23, v42
	v_bfe_u32 v47, v40, 1, 3
	v_lshlrev_b32_e32 v39, 2, v41
	v_xor_b32_e32 v39, v39, v47
	s_lshl_b32 s23, s23, 12
	v_lshlrev_b32_e32 v39, 4, v39
	v_lshl_add_u32 v39, v40, 7, v39
	v_lshl_add_u32 v39, v42, 12, v39
	s_mov_b32 m0, s23
	v_xor_b32_e32 v81, 16, v39
	v_xor_b32_e32 v82, 32, v39
	v_xor_b32_e32 v83, 48, v39
	v_cmp_gt_u32_e32 vcc, 32, v45
	v_mov_b32_e32 v34, 0xc1600000
	s_mov_b32 s16, 0x3fb8aa3b
	s_mov_b32 s17, 0x3f317218
	s_mov_b32 s20, 0x7fc00
	s_mov_b32 s21, 0xff800
	s_mov_b32 s22, 0x17f400
	s_lshl_b32 s24, 1, 16
	s_lshl_b32 s25, 2, 16
	s_lshl_b32 s26, 3, 16
	s_lshl_b32 s27, 8, 16
	s_lshl_b32 s28, 9, 16
	s_lshl_b32 s29, 10, 16
	s_lshl_b32 s30, 11, 16
	s_lshl_b32 s31, 16, 16
	s_lshl_b32 s32, 17, 16
	s_lshl_b32 s33, 18, 16
	s_lshl_b32 s34, 19, 16
	s_lshl_b32 s35, 24, 16
	s_lshl_b32 s36, 25, 16
	s_lshl_b32 s37, 26, 16
	s_lshl_b32 s38, 27, 16
	s_mov_b32 s14, 0x200000
	s_mov_b32 s15, 0x20000
	s_waitcnt lgkmcnt(0)
	s_mov_b32 s12, s6
	s_and_b32 s13, s7, 0xffff
	s_and_b32 s5, s5, 0xffff
	s_mov_b32 s6, 0x800000
	s_mov_b32 s7, s15
	s_and_b32 s9, s9, 0xffff
	s_mov_b32 s10, s6
	s_mov_b32 s11, s15
	buffer_load_dword v18, v1, s[12:15], s3 offen nt
	buffer_load_dword v19, v1, s[12:15], s3 offen offset:128 nt
	buffer_load_dword v20, v1, s[12:15], s3 offen offset:256 nt
	buffer_load_dword v21, v1, s[12:15], s3 offen offset:384 nt
	buffer_load_dword v22, v1, s[12:15], s3 offen offset:512 nt
	buffer_load_dword v23, v1, s[12:15], s3 offen offset:640 nt
	buffer_load_dword v24, v1, s[12:15], s3 offen offset:768 nt
	buffer_load_dword v25, v1, s[12:15], s3 offen offset:896 nt
	buffer_load_dword v26, v1, s[12:15], s3 offen offset:1024 nt
	buffer_load_dword v27, v1, s[12:15], s3 offen offset:1152 nt
	buffer_load_dword v28, v1, s[12:15], s3 offen offset:1280 nt
	buffer_load_dword v29, v1, s[12:15], s3 offen offset:1408 nt
	buffer_load_dword v30, v1, s[12:15], s3 offen offset:1536 nt
	buffer_load_dword v31, v1, s[12:15], s3 offen offset:1664 nt
	buffer_load_dword v32, v1, s[12:15], s3 offen offset:1792 nt
	buffer_load_dword v33, v1, s[12:15], s3 offen offset:1920 nt
	buffer_load_dwordx4 v35, s[4:7], 0 offen nt lds
	buffer_load_dwordx4 v86, s[4:7], s20 offen offset:1024 nt lds
	buffer_load_dwordx4 v35, s[4:7], s21 offen offset:2048 nt lds
	buffer_load_dwordx4 v86, s[4:7], s22 offen offset:3072 nt lds
	s_waitcnt vmcnt(4)
	v_max3_f32 v49, v18, v19, v20
	v_max3_f32 v50, v21, v22, v23
	v_max3_f32 v49, v49, v24, v25
	v_max3_f32 v50, v50, v26, v27
	v_max3_f32 v49, v49, v28, v29
	v_max3_f32 v50, v50, v30, v31
	v_max3_f32 v49, v49, v32, v33
	v_max_f32_e32 v49, v49, v50
	v_mov_b32_e32 v50, v49
	s_nop 1
	v_permlane32_swap_b32_e32 v49, v50
	v_max_f32_e32 v49, v49, v50
	v_fmamk_f32 v49, v49, 0x3fb8aa3b, v34
	v_fma_f32 v18, v18, s16, -v49
	v_exp_f32_e32 v18, v18
	v_fma_f32 v19, v19, s16, -v49
	v_exp_f32_e32 v19, v19
	v_fma_f32 v20, v20, s16, -v49
	v_exp_f32_e32 v20, v20
	v_fma_f32 v21, v21, s16, -v49
	v_exp_f32_e32 v21, v21
	v_fma_f32 v22, v22, s16, -v49
	v_exp_f32_e32 v22, v22
	v_fma_f32 v23, v23, s16, -v49
	v_exp_f32_e32 v23, v23
	v_fma_f32 v24, v24, s16, -v49
	v_exp_f32_e32 v24, v24
	v_fma_f32 v25, v25, s16, -v49
	v_exp_f32_e32 v25, v25
	v_fma_f32 v26, v26, s16, -v49
	v_exp_f32_e32 v26, v26
	v_fma_f32 v27, v27, s16, -v49
	v_exp_f32_e32 v27, v27
	v_fma_f32 v28, v28, s16, -v49
	v_exp_f32_e32 v28, v28
	v_fma_f32 v29, v29, s16, -v49
	v_exp_f32_e32 v29, v29
	v_fma_f32 v30, v30, s16, -v49
	v_exp_f32_e32 v30, v30
	v_fma_f32 v31, v31, s16, -v49
	v_exp_f32_e32 v31, v31
	v_fma_f32 v32, v32, s16, -v49
	v_exp_f32_e32 v32, v32
	v_fma_f32 v33, v33, s16, -v49
	v_exp_f32_e32 v33, v33
	v_add_f32_e32 v50, v18, v19
	v_add_f32_e32 v51, v20, v21
	v_add_f32_e32 v50, v50, v22
	v_add_f32_e32 v51, v51, v23
	v_add_f32_e32 v50, v50, v24
	v_add_f32_e32 v51, v51, v25
	v_add_f32_e32 v50, v50, v26
	v_add_f32_e32 v51, v51, v27
	v_add_f32_e32 v50, v50, v28
	v_add_f32_e32 v51, v51, v29
	v_add_f32_e32 v50, v50, v30
	v_add_f32_e32 v51, v51, v31
	v_add_f32_e32 v50, v50, v32
	v_add_f32_e32 v51, v51, v33
	v_add_f32_e32 v50, v50, v51
	v_mov_b32_e32 v51, v50
	s_nop 1
	v_permlane32_swap_b32_e32 v50, v51
	v_add_f32_e32 v50, v50, v51
	v_log_f32_e32 v50, v50
	v_cvt_pk_f16_f32 v40, v18, v19
	v_cvt_pk_f16_f32 v41, v20, v21
	v_cvt_pk_f16_f32 v42, v22, v23
	v_cvt_pk_f16_f32 v43, v24, v25
	v_cvt_pk_f16_f32 v44, v26, v27
	v_cvt_pk_f16_f32 v45, v28, v29
	v_cvt_pk_f16_f32 v46, v30, v31
	v_cvt_pk_f16_f32 v47, v32, v33
	v_add_f32_e32 v50, 0x41600000, v50
	v_mul_f32_e32 v50, 0xbf317218, v50
	v_cndmask_b32_e64 v51, v50, 1.0, vcc
	s_waitcnt vmcnt(0)
	ds_read_b128 v[2:5], v39
	ds_read_b128 v[6:9], v81
	ds_read_b128 v[10:13], v82
	ds_read_b128 v[14:17], v83
	s_waitcnt lgkmcnt(2)
	v_max3_f32 v52, v2, v3, v4
	v_max3_f32 v53, v5, v6, v7
	v_max_f32_e32 v52, v52, v8
	v_max_f32_e32 v53, v53, v9
	s_waitcnt lgkmcnt(0)
	v_max3_f32 v52, v52, v10, v11
	v_max3_f32 v53, v53, v12, v13
	v_max3_f32 v52, v52, v14, v15
	v_max3_f32 v53, v53, v16, v17
	v_max_f32_e32 v52, v52, v53
	v_mov_b32_e32 v53, v52
	s_nop 1
	v_permlane32_swap_b32_e32 v52, v53
	v_max_f32_e32 v52, v52, v53
	v_cndmask_b32_e32 v54, 1.0, v52, vcc
	v_fmamk_f32 v55, v52, 0x3fb8aa3b, v34
	v_fma_f32 v2, v2, s16, -v55
	v_mfma_f32_32x32x2_f32 v[64:79], v54, v51, 0
	v_exp_f32_e32 v2, v2
	v_fma_f32 v3, v3, s16, -v55
	v_exp_f32_e32 v3, v3
	v_fma_f32 v4, v4, s16, -v55
	v_exp_f32_e32 v4, v4
	v_fma_f32 v5, v5, s16, -v55
	v_exp_f32_e32 v5, v5
	v_fma_f32 v6, v6, s16, -v55
	v_exp_f32_e32 v6, v6
	v_fma_f32 v7, v7, s16, -v55
	v_exp_f32_e32 v7, v7
	v_fma_f32 v8, v8, s16, -v55
	v_exp_f32_e32 v8, v8
	v_fma_f32 v9, v9, s16, -v55
	v_exp_f32_e32 v9, v9
	v_fma_f32 v10, v10, s16, -v55
	v_exp_f32_e32 v10, v10
	v_cvt_pk_f16_f32 v56, v2, v3
	v_cvt_pk_f16_f32 v57, v4, v5
	v_cvt_pk_f16_f32 v58, v6, v7
	v_cvt_pk_f16_f32 v59, v8, v9
	v_fma_f32 v11, v11, s16, -v55
	v_exp_f32_e32 v11, v11
	v_fma_f32 v12, v12, s16, -v55
	v_exp_f32_e32 v12, v12
	v_mfma_f32_32x32x16_f16 v[18:33], v[56:59], v[40:43], 0
	v_fma_f32 v13, v13, s16, -v55
	v_exp_f32_e32 v13, v13
	v_fma_f32 v14, v14, s16, -v55
	v_exp_f32_e32 v14, v14
	v_fma_f32 v15, v15, s16, -v55
	v_exp_f32_e32 v15, v15
	v_fma_f32 v16, v16, s16, -v55
	v_exp_f32_e32 v16, v16
	v_fma_f32 v17, v17, s16, -v55
	v_exp_f32_e32 v17, v17
	v_cvt_pk_f16_f32 v60, v10, v11
	v_cvt_pk_f16_f32 v61, v12, v13
	v_cvt_pk_f16_f32 v62, v14, v15
	v_cvt_pk_f16_f32 v63, v16, v17
	s_nop 1
	v_mfma_f32_32x32x16_f16 v[18:33], v[60:63], v[44:47], v[18:33]
	s_nop 11
	v_log_f32_e32 v18, v18
	v_log_f32_e32 v19, v19
	v_log_f32_e32 v20, v20
	v_fmac_f32_e32 v64, s17, v18
	buffer_store_dword v64, v36, s[8:11], 0 offen
	v_log_f32_e32 v21, v21
	v_fmac_f32_e32 v65, s17, v19
	buffer_store_dword v65, v36, s[8:11], s24 offen
	v_log_f32_e32 v22, v22
	v_fmac_f32_e32 v66, s17, v20
	buffer_store_dword v66, v36, s[8:11], s25 offen
	v_log_f32_e32 v23, v23
	v_fmac_f32_e32 v67, s17, v21
	buffer_store_dword v67, v36, s[8:11], s26 offen
	v_log_f32_e32 v24, v24
	v_fmac_f32_e32 v68, s17, v22
	buffer_store_dword v68, v36, s[8:11], s27 offen
	v_log_f32_e32 v25, v25
	v_fmac_f32_e32 v69, s17, v23
	buffer_store_dword v69, v36, s[8:11], s28 offen
	v_log_f32_e32 v26, v26
	v_fmac_f32_e32 v70, s17, v24
	buffer_store_dword v70, v36, s[8:11], s29 offen
	v_log_f32_e32 v27, v27
	v_fmac_f32_e32 v71, s17, v25
	buffer_store_dword v71, v36, s[8:11], s30 offen
	v_log_f32_e32 v28, v28
	v_fmac_f32_e32 v72, s17, v26
	buffer_store_dword v72, v36, s[8:11], s31 offen
	v_log_f32_e32 v29, v29
	v_fmac_f32_e32 v73, s17, v27
	buffer_store_dword v73, v36, s[8:11], s32 offen
	v_log_f32_e32 v30, v30
	v_fmac_f32_e32 v74, s17, v28
	buffer_store_dword v74, v36, s[8:11], s33 offen
	v_log_f32_e32 v31, v31
	v_fmac_f32_e32 v75, s17, v29
	buffer_store_dword v75, v36, s[8:11], s34 offen
	v_log_f32_e32 v32, v32
	v_fmac_f32_e32 v76, s17, v30
	buffer_store_dword v76, v36, s[8:11], s35 offen
	v_log_f32_e32 v33, v33
	v_fmac_f32_e32 v77, s17, v31
	buffer_store_dword v77, v36, s[8:11], s36 offen
	v_fmac_f32_e32 v78, s17, v32
	buffer_store_dword v78, v36, s[8:11], s37 offen
	v_fmac_f32_e32 v79, s17, v33
	buffer_store_dword v79, v36, s[8:11], s38 offen
	s_endpgm

	.amdhsa_kernel _Z16sum_layer_kernelPKfS0_Pf
		.amdhsa_group_segment_fixed_size 18432
		.amdhsa_private_segment_fixed_size 0
		.amdhsa_kernarg_size 24
		.amdhsa_user_sgpr_count 2
		.amdhsa_user_sgpr_dispatch_ptr 0
		.amdhsa_user_sgpr_queue_ptr 0
		.amdhsa_user_sgpr_kernarg_segment_ptr 1
		.amdhsa_user_sgpr_dispatch_id 0
		.amdhsa_user_sgpr_kernarg_preload_length 0
		.amdhsa_user_sgpr_kernarg_preload_offset 0
		.amdhsa_user_sgpr_private_segment_size 0
		.amdhsa_uses_dynamic_stack 0
		.amdhsa_enable_private_segment 0
		.amdhsa_system_sgpr_workgroup_id_x 1
		.amdhsa_system_sgpr_workgroup_id_y 0
		.amdhsa_system_sgpr_workgroup_id_z 0
		.amdhsa_system_sgpr_workgroup_info 0
		.amdhsa_system_vgpr_workitem_id 0
		.amdhsa_next_free_vgpr 88
		.amdhsa_next_free_sgpr 44
		.amdhsa_accum_offset 88
		.amdhsa_reserve_vcc 1
		.amdhsa_float_round_mode_32 0
		.amdhsa_float_round_mode_16_64 0
		.amdhsa_float_denorm_mode_32 3
		.amdhsa_float_denorm_mode_16_64 3
		.amdhsa_dx10_clamp 1
		.amdhsa_ieee_mode 1
		.amdhsa_fp16_overflow 0
		.amdhsa_tg_split 0
		.amdhsa_exception_fp_ieee_invalid_op 0
		.amdhsa_exception_fp_denorm_src 0
		.amdhsa_exception_fp_ieee_div_zero 0
		.amdhsa_exception_fp_ieee_overflow 0
		.amdhsa_exception_fp_ieee_underflow 0
		.amdhsa_exception_fp_ieee_inexact 0
		.amdhsa_exception_int_div_zero 0
	.end_amdhsa_kernel

amdhsa.kernels:
  - .agpr_count:     0
    .args:
      - .address_space:  global
        .offset:         0
        .size:           8
        .value_kind:     global_buffer
      - .address_space:  global
        .offset:         8
        .size:           8
        .value_kind:     global_buffer
      - .address_space:  global
        .offset:         16
        .size:           8
        .value_kind:     global_buffer
    .group_segment_fixed_size: 18432
    .kernarg_segment_align: 8
    .kernarg_segment_size: 24
    .language:       OpenCL C
    .language_version:
      - 2
      - 0
    .max_flat_workgroup_size: 256
    .name:           _Z16sum_layer_kernelPKfS0_Pf
    .private_segment_fixed_size: 0
    .sgpr_count:     50
    .sgpr_spill_count: 0
    .symbol:         _Z16sum_layer_kernelPKfS0_Pf.kd
    .uniform_work_group_size: 1
    .uses_dynamic_stack: false
    .vgpr_count:     88
    .vgpr_spill_count: 0
    .wavefront_size: 64
